# grid barrier: non-leader CUs invalidate at arrival (L1 cannot refill while parked), XCD leader completes its invalidate before releasing locals; on top of attention LDS-DMA
# speedup vs baseline: 1.0031x; 1.0031x over previous
.LBB0_415:
	s_or_b64 exec, exec, s[10:11]
	v_cvt_f32_u32_e32 v5, v3
	s_waitcnt vmcnt(0)
	v_readfirstlane_b32 s2, v4
	v_sub_u32_e32 v4, 0, v3
	v_rcp_iflag_f32_e32 v5, v5
	v_add_u32_e32 v6, s2, v2
	v_mul_f32_e32 v5, 0x4f7ffffe, v5
	v_cvt_u32_f32_e32 v5, v5
	v_mul_lo_u32 v2, v4, v5
	v_mul_hi_u32 v2, v5, v2
	v_add_u32_e32 v2, v5, v2
	v_mul_hi_u32 v2, v6, v2
	v_mul_lo_u32 v4, v2, v3
	v_sub_u32_e32 v4, v6, v4
	v_add_u32_e32 v5, 1, v2
	v_cmp_ge_u32_e32 vcc, v4, v3
	s_nop 1
	v_cndmask_b32_e32 v2, v2, v5, vcc
	v_sub_u32_e32 v5, v4, v3
	v_cndmask_b32_e32 v4, v4, v5, vcc
	v_add_u32_e32 v5, 1, v2
	v_cmp_ge_u32_e32 vcc, v4, v3
	v_add_u32_e32 v4, 1, v6
	s_nop 0
	v_cndmask_b32_e32 v2, v2, v5, vcc
	v_mul_lo_u32 v5, v3, v2
	v_add_u32_e32 v3, v5, v3
	v_cmp_ne_u32_e32 vcc, v4, v3
	s_and_saveexec_b64 s[2:3], vcc
	s_xor_b64 s[8:9], exec, s[2:3]
	s_cbranch_execz .LBB0_429
	s_waitcnt lgkmcnt(0)
	buffer_inv sc1
	v_mov_b32_e32 v1, 0x2000
	global_load_dword v1, v1, s[6:7] offset:1024 sc1
	s_add_u32 s16, s6, 0x2400
	s_addc_u32 s17, s7, 0
	s_waitcnt vmcnt(0)
	v_cmp_eq_u32_e32 vcc, v1, v2
	s_and_saveexec_b64 s[10:11], vcc
	s_cbranch_execz .LBB0_428
	s_mov_b32 s2, 1
	s_mov_b64 s[18:19], 0
	v_mov_b32_e32 v1, 0
	s_branch .LBB0_419

.LBB0_428:
	s_or_b64 exec, exec, s[10:11]
	s_waitcnt vmcnt(0)
	s_waitcnt vmcnt(0)

.LBB0_446:
	s_or_b64 exec, exec, s[8:9]
	s_mov_b64 s[8:9], exec
	v_mbcnt_lo_u32_b32 v1, s8, 0
	v_mbcnt_hi_u32_b32 v1, s9, v1
	v_cmp_eq_u32_e32 vcc, 0, v1
	s_waitcnt vmcnt(0)
	buffer_inv sc1
	s_waitcnt vmcnt(0)
	s_and_saveexec_b64 s[10:11], vcc
	s_cbranch_execz .LBB0_448
	s_bcnt1_i32_b64 s2, s[8:9]
	v_mov_b32_e32 v1, 0x2000
	v_mov_b32_e32 v2, s2
	global_atomic_add v1, v2, s[6:7] offset:1024

.LBB0_500:
	s_or_b64 exec, exec, s[24:25]
	v_cvt_f32_u32_e32 v5, v3
	s_waitcnt vmcnt(0)
	v_readfirstlane_b32 s3, v4
	v_sub_u32_e32 v4, 0, v3
	v_rcp_iflag_f32_e32 v5, v5
	v_add_u32_e32 v6, s3, v1
	v_mul_f32_e32 v5, 0x4f7ffffe, v5
	v_cvt_u32_f32_e32 v5, v5
	v_mul_lo_u32 v1, v4, v5
	v_mul_hi_u32 v1, v5, v1
	v_add_u32_e32 v1, v5, v1
	v_mul_hi_u32 v1, v6, v1
	v_mul_lo_u32 v4, v1, v3
	v_sub_u32_e32 v4, v6, v4
	v_add_u32_e32 v5, 1, v1
	v_cmp_ge_u32_e32 vcc, v4, v3
	s_nop 1
	v_cndmask_b32_e32 v1, v1, v5, vcc
	v_sub_u32_e32 v5, v4, v3
	v_cndmask_b32_e32 v4, v4, v5, vcc
	v_add_u32_e32 v5, 1, v1
	v_cmp_ge_u32_e32 vcc, v4, v3
	v_add_u32_e32 v4, 1, v6
	s_nop 0
	v_cndmask_b32_e32 v1, v1, v5, vcc
	v_mul_lo_u32 v5, v3, v1
	v_add_u32_e32 v3, v5, v3
	v_cmp_ne_u32_e32 vcc, v4, v3
	s_and_saveexec_b64 s[4:5], vcc
	s_xor_b64 s[22:23], exec, s[4:5]
	s_cbranch_execz .LBB0_514
	s_waitcnt lgkmcnt(0)
	buffer_inv sc1
	v_mov_b32_e32 v2, 0x2000
	global_load_dword v2, v2, s[18:19] offset:1024 sc1
	s_add_u32 s26, s18, 0x2400
	s_addc_u32 s27, s19, 0
	s_waitcnt vmcnt(0)
	v_cmp_eq_u32_e32 vcc, v2, v1
	s_and_saveexec_b64 s[24:25], vcc
	s_cbranch_execz .LBB0_513
	s_mov_b32 s3, 1
	s_mov_b64 s[28:29], 0
	s_branch .LBB0_504

.LBB0_513:
	s_or_b64 exec, exec, s[24:25]
	s_waitcnt vmcnt(0)
	s_waitcnt vmcnt(0)

.LBB0_531:
	s_or_b64 exec, exec, s[4:5]
	s_mov_b64 s[22:23], exec
	v_mbcnt_lo_u32_b32 v1, s22, 0
	v_mbcnt_hi_u32_b32 v1, s23, v1
	v_cmp_eq_u32_e32 vcc, 0, v1
	s_waitcnt vmcnt(0)
	buffer_inv sc1
	s_waitcnt vmcnt(0)
	s_and_saveexec_b64 s[24:25], vcc
	s_cbranch_execz .LBB0_533
	s_bcnt1_i32_b64 s3, s[22:23]
	v_mov_b32_e32 v1, s3
	v_mov_b32_e32 v2, 0x2000
	global_atomic_add v2, v1, s[18:19] offset:1024

.LBB0_1642:
	s_or_b64 exec, exec, s[26:27]
	v_cvt_f32_u32_e32 v5, v3
	s_waitcnt vmcnt(0)
	v_readfirstlane_b32 s3, v4
	v_sub_u32_e32 v4, 0, v3
	v_rcp_iflag_f32_e32 v5, v5
	v_add_u32_e32 v6, s3, v1
	v_mul_f32_e32 v5, 0x4f7ffffe, v5
	v_cvt_u32_f32_e32 v5, v5
	v_mul_lo_u32 v1, v4, v5
	v_mul_hi_u32 v1, v5, v1
	v_add_u32_e32 v1, v5, v1
	v_mul_hi_u32 v1, v6, v1
	v_mul_lo_u32 v4, v1, v3
	v_sub_u32_e32 v4, v6, v4
	v_add_u32_e32 v5, 1, v1
	v_cmp_ge_u32_e32 vcc, v4, v3
	s_nop 1
	v_cndmask_b32_e32 v1, v1, v5, vcc
	v_sub_u32_e32 v5, v4, v3
	v_cndmask_b32_e32 v4, v4, v5, vcc
	v_add_u32_e32 v5, 1, v1
	v_cmp_ge_u32_e32 vcc, v4, v3
	v_add_u32_e32 v4, 1, v6
	s_nop 0
	v_cndmask_b32_e32 v1, v1, v5, vcc
	v_mul_lo_u32 v5, v3, v1
	v_add_u32_e32 v3, v5, v3
	v_cmp_ne_u32_e32 vcc, v4, v3
	s_and_saveexec_b64 s[4:5], vcc
	s_xor_b64 s[24:25], exec, s[4:5]
	s_cbranch_execz .LBB0_1656
	s_waitcnt lgkmcnt(0)
	buffer_inv sc1
	v_mov_b32_e32 v2, 0x2000
	global_load_dword v2, v2, s[22:23] offset:1024 sc1
	s_add_u32 s28, s22, 0x2400
	s_addc_u32 s29, s23, 0
	s_waitcnt vmcnt(0)
	v_cmp_eq_u32_e32 vcc, v2, v1
	s_and_saveexec_b64 s[26:27], vcc
	s_cbranch_execz .LBB0_1655
	s_mov_b32 s3, 1
	s_mov_b64 s[30:31], 0
	s_branch .LBB0_1646

.LBB0_1655:
	s_or_b64 exec, exec, s[26:27]
	s_waitcnt vmcnt(0)
	s_waitcnt vmcnt(0)

.LBB0_1673:
	s_or_b64 exec, exec, s[4:5]
	s_mov_b64 s[24:25], exec
	v_mbcnt_lo_u32_b32 v1, s24, 0
	v_mbcnt_hi_u32_b32 v1, s25, v1
	v_cmp_eq_u32_e32 vcc, 0, v1
	s_waitcnt vmcnt(0)
	buffer_inv sc1
	s_waitcnt vmcnt(0)
	s_and_saveexec_b64 s[26:27], vcc
	s_cbranch_execz .LBB0_1675
	s_bcnt1_i32_b64 s3, s[24:25]
	v_mov_b32_e32 v1, s3
	v_mov_b32_e32 v2, 0x2000
	global_atomic_add v2, v1, s[22:23] offset:1024

.LBB0_2295:
	s_or_b64 exec, exec, s[4:5]
	s_mov_b64 s[22:23], exec
	v_mbcnt_lo_u32_b32 v1, s22, 0
	v_mbcnt_hi_u32_b32 v1, s23, v1
	v_cmp_eq_u32_e32 vcc, 0, v1
	s_waitcnt vmcnt(0)
	buffer_inv sc1
	s_waitcnt vmcnt(0)
	s_and_saveexec_b64 s[24:25], vcc
	s_cbranch_execnz .LBB0_2296
	s_getpc_b64 s[98:99]
